# P1, P4 and P6 epilogue stores all without nt, on top of combo2
# speedup vs baseline: 1.0155x; 1.0059x over previous
; __device__ __forceinline__ unsigned cvt_pk_bf16(float lo, float hi) { unsigned r; asm volatile("v_cvt_pk_bf16_f32 %0, %1, %2" : "=v"(r) : "v"(lo), "v"(hi)); return r; }
;     __device__ __forceinline__ void operator()(const f32x4 (&acc)[2][2][4][2], const Unit& u, int wr, int wc, int fr, int fq) const {
;     ...
;         } else { const int col0 = (u.pn >= ch_tile0 + ch_tiles ? u.pn - ch_tiles / 2 : u.pn) * BM + cin;
; #pragma unroll
;             for (int ai = 0; ai < 2; ++ai)
; #pragma unroll
;                 for (int m = 0; m < 4; ++m) { bf16_t* rowp = O + (size_t)(row0 + ai * HALF + m * 16) * ldc + col0;
; #pragma unroll
;                     for (int bj = 0; bj < 2; ++bj) { const f32x4 v0 = acc[ai][bj][m][0], v1 = acc[ai][bj][m][1];
;                         u32x4 w; w.x = cvt_pk_bf16(v0[0], v0[1]); w.y = cvt_pk_bf16(v0[2], v0[3]); w.z = cvt_pk_bf16(v1[0], v1[1]); w.w = cvt_pk_bf16(v1[2], v1[3]);
;                         __builtin_nontemporal_store(w, (u32x4*)(rowp + bj * HALF)); } }
.LBB0_108:
	s_lshl_b32 s15, s45, 8
	s_add_i32 s17, s15, 0xfffff000
	s_cmpk_lt_i32 s45, 0x48
	s_cselect_b32 s15, s15, s17
	v_or_b32_e32 v156, s15, v135
	v_ashrrev_i32_e32 v157, 31, v156
	v_mov_b64_e32 v[154:155], s[10:11]
	v_mad_i64_i32 v[170:171], s[22:23], v144, s44, v[154:155]
	v_lshlrev_b64 v[156:157], 1, v[156:157]
	v_lshl_add_u64 v[174:175], v[170:171], 0, v[156:157]
	v_cvt_pk_bf16_f32 v170, v126, v127
	v_cvt_pk_bf16_f32 v171, v128, v129
	v_cvt_pk_bf16_f32 v172, v122, v123
	v_cvt_pk_bf16_f32 v173, v124, v125
	global_store_dwordx4 v[174:175], v[170:173], off
	s_nop 1
	v_cvt_pk_bf16_f32 v170, v118, v119
	v_cvt_pk_bf16_f32 v171, v120, v121
	v_cvt_pk_bf16_f32 v172, v114, v115
	v_cvt_pk_bf16_f32 v173, v116, v117
	global_store_dwordx4 v[174:175], v[170:173], off offset:256
	s_nop 1
	v_mad_i64_i32 v[170:171], s[22:23], v168, s44, v[154:155]
	v_lshl_add_u64 v[174:175], v[170:171], 0, v[156:157]
	v_cvt_pk_bf16_f32 v170, v110, v111
	v_cvt_pk_bf16_f32 v171, v112, v113
	v_cvt_pk_bf16_f32 v172, v106, v107
	v_cvt_pk_bf16_f32 v173, v108, v109
	global_store_dwordx4 v[174:175], v[170:173], off
	s_nop 1
	v_cvt_pk_bf16_f32 v170, v102, v103
	v_cvt_pk_bf16_f32 v171, v104, v105
	v_cvt_pk_bf16_f32 v172, v94, v95
	v_cvt_pk_bf16_f32 v173, v96, v97
	global_store_dwordx4 v[174:175], v[170:173], off offset:256
	s_nop 1
	v_mad_i64_i32 v[170:171], s[22:23], v167, s44, v[154:155]
	v_lshl_add_u64 v[174:175], v[170:171], 0, v[156:157]
	v_cvt_pk_bf16_f32 v170, v98, v99
	v_cvt_pk_bf16_f32 v171, v100, v101
	v_cvt_pk_bf16_f32 v172, v90, v91
	v_cvt_pk_bf16_f32 v173, v92, v93
	global_store_dwordx4 v[174:175], v[170:173], off
	s_nop 1
	v_cvt_pk_bf16_f32 v170, v86, v87
	v_cvt_pk_bf16_f32 v171, v88, v89
	v_cvt_pk_bf16_f32 v172, v78, v79
	v_cvt_pk_bf16_f32 v173, v80, v81
	global_store_dwordx4 v[174:175], v[170:173], off offset:256
	s_nop 1
	v_mad_i64_i32 v[170:171], s[22:23], v166, s44, v[154:155]
	v_lshl_add_u64 v[174:175], v[170:171], 0, v[156:157]
	v_cvt_pk_bf16_f32 v170, v82, v83
	v_cvt_pk_bf16_f32 v171, v84, v85
	v_cvt_pk_bf16_f32 v172, v74, v75
	v_cvt_pk_bf16_f32 v173, v76, v77
	global_store_dwordx4 v[174:175], v[170:173], off
	s_nop 1
	v_cvt_pk_bf16_f32 v170, v70, v71
	v_cvt_pk_bf16_f32 v171, v72, v73
	v_cvt_pk_bf16_f32 v172, v66, v67
	v_cvt_pk_bf16_f32 v173, v68, v69
	global_store_dwordx4 v[174:175], v[170:173], off offset:256
	s_nop 1
	v_mad_i64_i32 v[170:171], s[22:23], v165, s44, v[154:155]
	v_lshl_add_u64 v[174:175], v[170:171], 0, v[156:157]
	v_cvt_pk_bf16_f32 v170, v62, v63
	v_cvt_pk_bf16_f32 v171, v64, v65
	v_cvt_pk_bf16_f32 v172, v58, v59
	v_cvt_pk_bf16_f32 v173, v60, v61
	global_store_dwordx4 v[174:175], v[170:173], off
	s_nop 1
	v_cvt_pk_bf16_f32 v170, v54, v55
	v_cvt_pk_bf16_f32 v171, v56, v57
	v_cvt_pk_bf16_f32 v172, v46, v47
	v_cvt_pk_bf16_f32 v173, v48, v49
	global_store_dwordx4 v[174:175], v[170:173], off offset:256
	s_nop 1
	v_mad_i64_i32 v[170:171], s[22:23], v164, s44, v[154:155]
	v_lshl_add_u64 v[174:175], v[170:171], 0, v[156:157]
	v_cvt_pk_bf16_f32 v170, v50, v51
	v_cvt_pk_bf16_f32 v171, v52, v53
	v_cvt_pk_bf16_f32 v172, v42, v43
	v_cvt_pk_bf16_f32 v173, v44, v45
	global_store_dwordx4 v[174:175], v[170:173], off
	s_nop 1
	v_cvt_pk_bf16_f32 v170, v38, v39
	v_cvt_pk_bf16_f32 v171, v40, v41
	v_cvt_pk_bf16_f32 v172, v30, v31
	v_cvt_pk_bf16_f32 v173, v32, v33
	global_store_dwordx4 v[174:175], v[170:173], off offset:256
	s_nop 1
	v_mad_i64_i32 v[170:171], s[22:23], v163, s44, v[154:155]
	v_lshl_add_u64 v[174:175], v[170:171], 0, v[156:157]
	v_cvt_pk_bf16_f32 v170, v34, v35
	v_cvt_pk_bf16_f32 v171, v36, v37
	v_cvt_pk_bf16_f32 v172, v26, v27
	v_cvt_pk_bf16_f32 v173, v28, v29
	global_store_dwordx4 v[174:175], v[170:173], off
	v_mad_i64_i32 v[154:155], s[22:23], v162, s44, v[154:155]
	s_nop 0
	v_cvt_pk_bf16_f32 v170, v22, v23
	v_cvt_pk_bf16_f32 v171, v24, v25
	v_cvt_pk_bf16_f32 v172, v14, v15
	v_cvt_pk_bf16_f32 v173, v16, v17
	global_store_dwordx4 v[174:175], v[170:173], off offset:256
	s_nop 1
	v_lshl_add_u64 v[170:171], v[154:155], 0, v[156:157]
	v_cvt_pk_bf16_f32 v154, v18, v19
	v_cvt_pk_bf16_f32 v155, v20, v21
	v_cvt_pk_bf16_f32 v156, v10, v11
	v_cvt_pk_bf16_f32 v157, v12, v13
	global_store_dwordx4 v[170:171], v[154:157], off
	s_nop 1
	v_cvt_pk_bf16_f32 v154, v6, v7
	v_cvt_pk_bf16_f32 v155, v8, v9
	v_cvt_pk_bf16_f32 v156, v2, v3
	v_cvt_pk_bf16_f32 v157, v4, v5
	global_store_dwordx4 v[170:171], v[154:157], off offset:256
	s_cbranch_execnz .LBB0_107
; __device__ __forceinline__ unsigned cvt_pk_bf16(float lo, float hi) { unsigned r; asm volatile("v_cvt_pk_bf16_f32 %0, %1, %2" : "=v"(r) : "v"(lo), "v"(hi)); return r; }
;     __device__ __forceinline__ void operator()(const f32x4 (&acc)[2][2][4][2], const Unit& u, int wr, int wc, int fr, int fq) const {
;     ...
;         if (chv) { const int col0 = u_col0 + (u.pn - ch_tile0) * HALF + cin;
; #pragma unroll
;             for (int ai = 0; ai < 2; ++ai)
; #pragma unroll
;                 for (int m = 0; m < 4; ++m) { const f32x4 v0 = acc[ai][0][m][0] * acc[ai][1][m][0], v1 = acc[ai][0][m][1] * acc[ai][1][m][1];
;                     u32x4 w; w.x = cvt_pk_bf16(v0[0], v0[1]); w.y = cvt_pk_bf16(v0[2], v0[3]); w.z = cvt_pk_bf16(v1[0], v1[1]); w.w = cvt_pk_bf16(v1[2], v1[3]);
;                     __builtin_nontemporal_store(w, (u32x4*)(O + (size_t)(row0 + ai * HALF + m * 16) * ldc + col0)); }
.LBB0_109:
	v_pk_mul_f32 v[118:119], v[126:127], v[118:119]
	s_lshl_b32 s15, s45, 7
	v_pk_mul_f32 v[120:121], v[128:129], v[120:121]
	v_pk_mul_f32 v[124:125], v[124:125], v[116:117]
	v_pk_mul_f32 v[116:117], v[122:123], v[114:115]
	v_cvt_pk_bf16_f32 v114, v118, v119
	v_mov_b64_e32 v[118:119], s[10:11]
	v_cvt_pk_bf16_f32 v115, v120, v121
	v_mad_i64_i32 v[120:121], s[22:23], v144, s44, v[118:119]
	v_add_lshl_u32 v144, v158, s15, 1
	v_lshl_add_u64 v[120:121], v[120:121], 0, v[144:145]
	v_pk_mul_f32 v[102:103], v[110:111], v[102:103]
	v_cvt_pk_bf16_f32 v116, v116, v117
	v_cvt_pk_bf16_f32 v117, v124, v125
	global_store_dwordx4 v[120:121], v[114:117], off
	v_pk_mul_f32 v[108:109], v[108:109], v[96:97]
	v_pk_mul_f32 v[96:97], v[106:107], v[94:95]
	v_cvt_pk_bf16_f32 v94, v102, v103
	v_mad_i64_i32 v[102:103], s[22:23], v168, s44, v[118:119]
	v_lshl_add_u64 v[102:103], v[102:103], 0, v[144:145]
	v_pk_mul_f32 v[86:87], v[98:99], v[86:87]
	v_pk_mul_f32 v[104:105], v[112:113], v[104:105]
	v_pk_mul_f32 v[92:93], v[92:93], v[80:81]
	v_cvt_pk_bf16_f32 v95, v104, v105
	v_cvt_pk_bf16_f32 v96, v96, v97
	v_cvt_pk_bf16_f32 v97, v108, v109
	global_store_dwordx4 v[102:103], v[94:97], off
	v_pk_mul_f32 v[80:81], v[90:91], v[78:79]
	v_cvt_pk_bf16_f32 v78, v86, v87
	v_mad_i64_i32 v[86:87], s[22:23], v167, s44, v[118:119]
	v_lshl_add_u64 v[86:87], v[86:87], 0, v[144:145]
	v_pk_mul_f32 v[70:71], v[82:83], v[70:71]
	v_pk_mul_f32 v[88:89], v[100:101], v[88:89]
	v_pk_mul_f32 v[76:77], v[76:77], v[68:69]
	v_cvt_pk_bf16_f32 v79, v88, v89
	v_cvt_pk_bf16_f32 v80, v80, v81
	v_cvt_pk_bf16_f32 v81, v92, v93
	global_store_dwordx4 v[86:87], v[78:81], off
	v_pk_mul_f32 v[68:69], v[74:75], v[66:67]
	v_cvt_pk_bf16_f32 v66, v70, v71
	v_mad_i64_i32 v[70:71], s[22:23], v166, s44, v[118:119]
	v_lshl_add_u64 v[70:71], v[70:71], 0, v[144:145]
	v_pk_mul_f32 v[54:55], v[62:63], v[54:55]
	v_pk_mul_f32 v[72:73], v[84:85], v[72:73]
	v_pk_mul_f32 v[60:61], v[60:61], v[48:49]
	v_cvt_pk_bf16_f32 v67, v72, v73
	v_cvt_pk_bf16_f32 v68, v68, v69
	v_cvt_pk_bf16_f32 v69, v76, v77
	global_store_dwordx4 v[70:71], v[66:69], off
	v_pk_mul_f32 v[48:49], v[58:59], v[46:47]
	v_cvt_pk_bf16_f32 v46, v54, v55
	v_mad_i64_i32 v[54:55], s[22:23], v165, s44, v[118:119]
	v_lshl_add_u64 v[54:55], v[54:55], 0, v[144:145]
	v_pk_mul_f32 v[38:39], v[50:51], v[38:39]
	v_pk_mul_f32 v[56:57], v[64:65], v[56:57]
	v_pk_mul_f32 v[44:45], v[44:45], v[32:33]
	v_cvt_pk_bf16_f32 v47, v56, v57
	v_cvt_pk_bf16_f32 v48, v48, v49
	v_cvt_pk_bf16_f32 v49, v60, v61
	global_store_dwordx4 v[54:55], v[46:49], off
	v_pk_mul_f32 v[32:33], v[42:43], v[30:31]
	v_cvt_pk_bf16_f32 v30, v38, v39
	v_mad_i64_i32 v[38:39], s[22:23], v164, s44, v[118:119]
	v_lshl_add_u64 v[38:39], v[38:39], 0, v[144:145]
	v_pk_mul_f32 v[22:23], v[34:35], v[22:23]
	v_pk_mul_f32 v[40:41], v[52:53], v[40:41]
	v_pk_mul_f32 v[28:29], v[28:29], v[16:17]
	v_cvt_pk_bf16_f32 v31, v40, v41
	v_cvt_pk_bf16_f32 v32, v32, v33
	v_cvt_pk_bf16_f32 v33, v44, v45
	global_store_dwordx4 v[38:39], v[30:33], off
	v_pk_mul_f32 v[16:17], v[26:27], v[14:15]
	v_cvt_pk_bf16_f32 v14, v22, v23
	v_mad_i64_i32 v[22:23], s[22:23], v163, s44, v[118:119]
	v_lshl_add_u64 v[22:23], v[22:23], 0, v[144:145]
	v_pk_mul_f32 v[6:7], v[18:19], v[6:7]
	v_pk_mul_f32 v[24:25], v[36:37], v[24:25]
	v_pk_mul_f32 v[12:13], v[12:13], v[4:5]
	v_cvt_pk_bf16_f32 v15, v24, v25
	v_cvt_pk_bf16_f32 v16, v16, v17
	v_cvt_pk_bf16_f32 v17, v28, v29
	global_store_dwordx4 v[22:23], v[14:17], off
	v_pk_mul_f32 v[4:5], v[10:11], v[2:3]
	v_cvt_pk_bf16_f32 v2, v6, v7
	v_mad_i64_i32 v[6:7], s[22:23], v162, s44, v[118:119]
	v_lshl_add_u64 v[6:7], v[6:7], 0, v[144:145]
	v_pk_mul_f32 v[8:9], v[20:21], v[8:9]
	s_nop 0
	v_cvt_pk_bf16_f32 v3, v8, v9
	v_cvt_pk_bf16_f32 v4, v4, v5
	v_cvt_pk_bf16_f32 v5, v12, v13
	global_store_dwordx4 v[6:7], v[2:5], off
	s_andn2_b64 vcc, exec, s[4:5]
	s_mov_b64 s[4:5], -1
	s_cbranch_vccnz .LBB0_98
